# KV2 consumer epilogue rewritten: tables loaded once before K loop, 8 stores back to back (was 8 serial load-wait-store trips)
# speedup vs baseline: 1.0000x; 1.0000x over previous
.LBB3_36:
	s_cmpk_lt_u32 s27, 0x100
	s_cbranch_scc0 .LBB3_63
	s_lshr_b32 s2, s27, 1
	v_lshlrev_b32_e32 v1, 6, v0
	v_and_b32_e32 v2, 48, v0
	s_movk_i32 s3, 0x3c0
	v_and_or_b32 v2, v1, s3, v2
	v_lshlrev_b32_e32 v1, 2, v0
	s_and_b32 s3, s2, 64
	s_and_b32 s2, s2, 32
	v_and_b32_e32 v3, 32, v1
	s_lshl_b32 s8, s3, 7
	s_lshl_b32 s9, s2, 7
	v_and_b32_e32 v90, 15, v0
	v_lshl_or_b32 v90, s26, 7, v90
	v_or_b32_e32 v90, s3, v90
	v_lshrrev_b32_e32 v91, 2, v0
	v_and_b32_e32 v91, 12, v91
	v_lshl_or_b32 v91, s24, 6, v91
	v_or_b32_e32 v91, s2, v91
	s_movk_i32 s33, 0x1000
	s_cmp_lg_u64 s[22:23], 0
	s_cselect_b32 s28, s20, s18
	s_cselect_b32 s29, s21, s19
	s_cselect_b32 s30, s18, s20
	s_cselect_b32 s31, s19, s21
	s_cselect_b32 s32, 0x2000, 0
	s_cselect_b32 s33, 0x400, s33
	s_cselect_b32 s34, 9, 11
	s_cselect_b32 s35, 1.0, 0x3e38aa3b
	s_cselect_b32 s36, s16, s14
	s_cselect_b32 s37, s17, s15
	s_cselect_b32 s38, s25, s12
	s_lshl_b32 s38, s38, 19
	s_add_u32 s36, s36, s38
	s_addc_u32 s37, s37, 0
	s_lshl_b32 s39, 16, s34
	v_lshl_add_u32 v92, v90, 2, s32
	v_lshl_add_u32 v93, v91, 2, s33
	global_load_dword v100, v92, s[28:29]
	global_load_dword v101, v92, s[28:29] offset:64
	global_load_dword v102, v92, s[28:29] offset:128
	global_load_dword v103, v92, s[28:29] offset:192
	global_load_dwordx4 v[104:107], v93, s[30:31]
	global_load_dwordx4 v[108:111], v93, s[30:31] offset:64
	v_lshlrev_b32_e32 v94, s34, v90
	v_lshl_add_u32 v95, v91, 1, v94
	v_add_u32_e32 v96, s39, v95
	v_add_u32_e32 v97, s39, v96
	v_add_u32_e32 v98, s39, v97
	v_bitop3_b32 v1, v2, s8, v3 bitop3:0xde
	v_bitop3_b32 v34, v2, s9, v3 bitop3:0xde
	v_mov_b32_e32 v2, 0
	s_mov_b32 s9, 0
	s_mov_b32 s8, 16
	v_mov_b32_e32 v3, v2
	v_mov_b32_e32 v4, v2
	v_mov_b32_e32 v5, v2
	v_mov_b32_e32 v6, v2
	v_mov_b32_e32 v7, v2
	v_mov_b32_e32 v8, v2
	v_mov_b32_e32 v9, v2
	v_mov_b32_e32 v10, v2
	v_mov_b32_e32 v11, v2
	v_mov_b32_e32 v12, v2
	v_mov_b32_e32 v13, v2
	v_mov_b32_e32 v14, v2
	v_mov_b32_e32 v15, v2
	v_mov_b32_e32 v16, v2
	v_mov_b32_e32 v17, v2
	v_mov_b32_e32 v18, v2
	v_mov_b32_e32 v19, v2
	v_mov_b32_e32 v20, v2
	v_mov_b32_e32 v21, v2
	v_mov_b32_e32 v22, v2
	v_mov_b32_e32 v23, v2
	v_mov_b32_e32 v24, v2
	v_mov_b32_e32 v25, v2
	v_mov_b32_e32 v26, v2
	v_mov_b32_e32 v27, v2
	v_mov_b32_e32 v28, v2
	v_mov_b32_e32 v29, v2
	v_mov_b32_e32 v30, v2
	v_mov_b32_e32 v31, v2
	v_mov_b32_e32 v32, v2
	v_mov_b32_e32 v33, v2
.LBB3_38:
	s_barrier
	v_add_u32_e32 v35, s9, v1
	v_add_u32_e32 v76, s9, v34
	ds_read_b128 v[36:39], v76 offset:16384
	ds_read_b128 v[40:43], v35
	ds_read_b128 v[44:47], v35 offset:1024
	ds_read_b128 v[48:51], v76 offset:17408
	ds_read_b128 v[52:55], v35 offset:2048
	ds_read_b128 v[56:59], v35 offset:3072
	ds_read_b128 v[60:63], v35 offset:4096
	ds_read_b128 v[64:67], v35 offset:5120
	ds_read_b128 v[68:71], v35 offset:6144
	ds_read_b128 v[72:75], v35 offset:7168
	s_waitcnt lgkmcnt(8)
	v_mfma_f32_16x16x32_f16 v[30:33], v[36:39], v[40:43], v[30:33]
	s_addk_i32 s9, 0x6000
	s_cmp_lg_u32 s9, 0x12000
	s_cselect_b32 s9, s9, 0
	s_waitcnt lgkmcnt(5)
	v_mfma_f32_16x16x32_f16 v[22:25], v[36:39], v[52:55], v[22:25]
	s_add_i32 s8, s8, -1
	s_cmp_eq_u32 s8, 0
	s_waitcnt lgkmcnt(3)
	v_mfma_f32_16x16x32_f16 v[14:17], v[36:39], v[60:63], v[14:17]
	s_waitcnt lgkmcnt(1)
	v_mfma_f32_16x16x32_f16 v[6:9], v[36:39], v[68:71], v[6:9]
	ds_read_b128 v[36:39], v76 offset:18432
	ds_read_b128 v[76:79], v76 offset:19456
	s_waitcnt lgkmcnt(1)
	v_mfma_f32_16x16x32_f16 v[26:29], v[36:39], v[40:43], v[26:29]
	v_mfma_f32_16x16x32_f16 v[18:21], v[36:39], v[52:55], v[18:21]
	v_mfma_f32_16x16x32_f16 v[10:13], v[36:39], v[60:63], v[10:13]
	v_mfma_f32_16x16x32_f16 v[2:5], v[36:39], v[68:71], v[2:5]
	v_mfma_f32_16x16x32_f16 v[30:33], v[48:51], v[44:47], v[30:33]
	v_mfma_f32_16x16x32_f16 v[22:25], v[48:51], v[56:59], v[22:25]
	v_mfma_f32_16x16x32_f16 v[14:17], v[48:51], v[64:67], v[14:17]
	v_mfma_f32_16x16x32_f16 v[6:9], v[48:51], v[72:75], v[6:9]
	s_waitcnt lgkmcnt(0)
	v_mfma_f32_16x16x32_f16 v[26:29], v[76:79], v[44:47], v[26:29]
	v_mfma_f32_16x16x32_f16 v[18:21], v[76:79], v[56:59], v[18:21]
	v_mfma_f32_16x16x32_f16 v[10:13], v[76:79], v[64:67], v[10:13]
	v_mfma_f32_16x16x32_f16 v[2:5], v[76:79], v[72:75], v[2:5]
	s_cbranch_scc0 .LBB3_38
	s_nop 7
	s_nop 7
	s_waitcnt vmcnt(0)
	v_fma_f32 v30, v100, v104, v30
	v_fma_f32 v31, v100, v105, v31
	v_fma_f32 v32, v100, v106, v32
	v_fma_f32 v33, v100, v107, v33
	v_mul_f32_e32 v30, s35, v30
	v_mul_f32_e32 v31, s35, v31
	v_mul_f32_e32 v32, s35, v32
	v_mul_f32_e32 v33, s35, v33
	v_cvt_pk_f16_f32 v30, v30, v31
	v_cvt_pk_f16_f32 v31, v32, v33
	global_store_dwordx2 v95, v[30:31], s[36:37]
	v_fma_f32 v26, v100, v108, v26
	v_fma_f32 v27, v100, v109, v27
	v_fma_f32 v28, v100, v110, v28
	v_fma_f32 v29, v100, v111, v29
	v_mul_f32_e32 v26, s35, v26
	v_mul_f32_e32 v27, s35, v27
	v_mul_f32_e32 v28, s35, v28
	v_mul_f32_e32 v29, s35, v29
	v_cvt_pk_f16_f32 v26, v26, v27
	v_cvt_pk_f16_f32 v27, v28, v29
	global_store_dwordx2 v95, v[26:27], s[36:37] offset:32
	v_fma_f32 v22, v101, v104, v22
	v_fma_f32 v23, v101, v105, v23
	v_fma_f32 v24, v101, v106, v24
	v_fma_f32 v25, v101, v107, v25
	v_mul_f32_e32 v22, s35, v22
	v_mul_f32_e32 v23, s35, v23
	v_mul_f32_e32 v24, s35, v24
	v_mul_f32_e32 v25, s35, v25
	v_cvt_pk_f16_f32 v22, v22, v23
	v_cvt_pk_f16_f32 v23, v24, v25
	global_store_dwordx2 v96, v[22:23], s[36:37]
	v_fma_f32 v18, v101, v108, v18
	v_fma_f32 v19, v101, v109, v19
	v_fma_f32 v20, v101, v110, v20
	v_fma_f32 v21, v101, v111, v21
	v_mul_f32_e32 v18, s35, v18
	v_mul_f32_e32 v19, s35, v19
	v_mul_f32_e32 v20, s35, v20
	v_mul_f32_e32 v21, s35, v21
	v_cvt_pk_f16_f32 v18, v18, v19
	v_cvt_pk_f16_f32 v19, v20, v21
	global_store_dwordx2 v96, v[18:19], s[36:37] offset:32
	v_fma_f32 v14, v102, v104, v14
	v_fma_f32 v15, v102, v105, v15
	v_fma_f32 v16, v102, v106, v16
	v_fma_f32 v17, v102, v107, v17
	v_mul_f32_e32 v14, s35, v14
	v_mul_f32_e32 v15, s35, v15
	v_mul_f32_e32 v16, s35, v16
	v_mul_f32_e32 v17, s35, v17
	v_cvt_pk_f16_f32 v14, v14, v15
	v_cvt_pk_f16_f32 v15, v16, v17
	global_store_dwordx2 v97, v[14:15], s[36:37]
	v_fma_f32 v10, v102, v108, v10
	v_fma_f32 v11, v102, v109, v11
	v_fma_f32 v12, v102, v110, v12
	v_fma_f32 v13, v102, v111, v13
	v_mul_f32_e32 v10, s35, v10
	v_mul_f32_e32 v11, s35, v11
	v_mul_f32_e32 v12, s35, v12
	v_mul_f32_e32 v13, s35, v13
	v_cvt_pk_f16_f32 v10, v10, v11
	v_cvt_pk_f16_f32 v11, v12, v13
	global_store_dwordx2 v97, v[10:11], s[36:37] offset:32
	v_fma_f32 v6, v103, v104, v6
	v_fma_f32 v7, v103, v105, v7
	v_fma_f32 v8, v103, v106, v8
	v_fma_f32 v9, v103, v107, v9
	v_mul_f32_e32 v6, s35, v6
	v_mul_f32_e32 v7, s35, v7
	v_mul_f32_e32 v8, s35, v8
	v_mul_f32_e32 v9, s35, v9
	v_cvt_pk_f16_f32 v6, v6, v7
	v_cvt_pk_f16_f32 v7, v8, v9
	global_store_dwordx2 v98, v[6:7], s[36:37]
	v_fma_f32 v2, v103, v108, v2
	v_fma_f32 v3, v103, v109, v3
	v_fma_f32 v4, v103, v110, v4
	v_fma_f32 v5, v103, v111, v5
	v_mul_f32_e32 v2, s35, v2
	v_mul_f32_e32 v3, s35, v3
	v_mul_f32_e32 v4, s35, v4
	v_mul_f32_e32 v5, s35, v5
	v_cvt_pk_f16_f32 v2, v2, v3
	v_cvt_pk_f16_f32 v3, v4, v5
	global_store_dwordx2 v98, v[2:3], s[36:37] offset:32
